# queue: next item index also prefetched in the last trip of the weight-conversion items (on top of v77)
# baseline (speedup 1.0000x reference)
.LBB0_416:
	s_or_b64 exec, exec, s[10:11]
	s_waitcnt lgkmcnt(0)
	s_barrier
	ds_read_b32 v2, v213
	s_xor_b64 s[10:11], s[8:9], -1
	s_mov_b64 s[8:9], -1
	s_and_b64 vcc, exec, s[10:11]
	s_waitcnt lgkmcnt(0)
	v_readfirstlane_b32 s54, v2
	s_cbranch_vccz .LBB0_500
	s_mov_b64 s[8:9], 0
	s_cmpk_gt_i32 s54, 0x413
	s_mov_b64 s[10:11], 0
	s_cbranch_scc1 .LBB0_500
	s_bitcmp1_b32 s5, 0
	s_cselect_b64 s[100:101], -1, 0
	s_and_b64 s[100:101], s[100:101], s[6:7]
	s_cmp_lg_u64 s[100:101], 0
	s_cselect_b32 s98, 1, 2
	v_writelane_b32 v255, s98, 20
	s_cmpk_gt_i32 s54, 0x155
	s_mov_b64 s[10:11], -1
	s_cbranch_scc0 .LBB0_487
	s_cmpk_gt_u32 s54, 0x2ab
	s_cbranch_scc0 .LBB0_474
	s_cmpk_gt_u32 s54, 0x401
	s_cbranch_scc0 .LBB0_461
	s_cmpk_gt_u32 s54, 0x407
	s_cbranch_scc0 .LBB0_448
	s_cmpk_gt_u32 s54, 0x40d
	s_mul_i32 s1, s54, 6
	s_cbranch_scc0 .LBB0_435
	s_add_i32 s10, s1, 0xffffe7b2
	s_add_i32 s0, s1, 0xffffe7ac
	s_min_u32 s34, s10, 32
	v_mov_b32_e32 v2, v0
	s_cmp_ge_u32 s0, s34
	s_cbranch_scc1 .LBB0_434
	v_and_b32_e32 v4, -16, v2
	v_readlane_b32 s10, v255, 17
	v_ashrrev_i32_e32 v5, 31, v4
	v_readlane_b32 s11, v255, 18
	v_readlane_b32 s44, v255, 9
	v_lshlrev_b32_e32 v8, 2, v2
	v_lshl_add_u64 v[202:203], s[10:11], 0, v[4:5]
	s_mul_i32 s10, s54, 0x180
	v_lshlrev_b64 v[6:7], 13, v[4:5]
	v_readlane_b32 s46, v255, 11
	v_readlane_b32 s47, v255, 12
	s_add_i32 s10, s10, 0xfff9eb00
	v_and_or_b32 v2, v8, 60, s10
	v_lshl_add_u64 v[196:197], s[46:47], 0, v[6:7]
	v_readlane_b32 s45, v255, 10
	s_branch .LBB0_426

.LBB0_430:
	s_waitcnt vmcnt(15)
	v_mul_f32_e32 v208, 0x42000000, v132
	s_waitcnt vmcnt(14)
	v_mul_f32_e32 v132, 0x42000000, v136
	v_cvt_pk_fp8_f32 v208, v208, v132
	s_waitcnt vmcnt(13)
	v_mul_f32_e32 v132, 0x42000000, v140
	s_waitcnt vmcnt(11)
	v_mul_f32_e32 v209, 0x42000000, v148
	s_waitcnt vmcnt(10)
	v_mul_f32_e32 v140, 0x42000000, v152
	v_cvt_pk_fp8_f32 v209, v209, v140
	v_mul_f32_e32 v136, 0x42000000, v144
	v_cvt_pk_fp8_f32 v208, v132, v136 op_sel:[0,0,1]
	s_waitcnt vmcnt(9)
	v_mul_f32_e32 v132, 0x42000000, v156
	s_waitcnt vmcnt(8)
	v_mul_f32_e32 v136, 0x42000000, v160
	v_cvt_pk_fp8_f32 v209, v132, v136 op_sel:[0,0,1]
	s_waitcnt vmcnt(7)
	v_mul_f32_e32 v210, 0x42000000, v164
	s_waitcnt vmcnt(6)
	v_mul_f32_e32 v132, 0x42000000, v168
	v_cvt_pk_fp8_f32 v210, v210, v132
	s_waitcnt vmcnt(3)
	v_mul_f32_e32 v211, 0x42000000, v180
	s_waitcnt vmcnt(2)
	v_mul_f32_e32 v140, 0x42000000, v184
	v_cvt_pk_fp8_f32 v211, v211, v140
	v_mul_f32_e32 v132, 0x42000000, v172
	v_mul_f32_e32 v136, 0x42000000, v176
	v_cvt_pk_fp8_f32 v210, v132, v136 op_sel:[0,0,1]
	s_waitcnt vmcnt(1)
	v_mul_f32_e32 v132, 0x42000000, v188
	s_waitcnt vmcnt(0)
	s_cmp_lg_u32 s32, 0
	s_cbranch_scc1 .Lmy_cpf0
	s_add_i32 s98, s0, 3
	s_cmp_lt_u32 s98, s34
	s_cbranch_scc1 .Lmy_cpf0
	v_readlane_b32 s32, v255, 20
	v_readlane_b32 s98, v255, 15
	v_readlane_b32 s99, v255, 16
	s_cmp_eq_u32 s32, 1
	s_cselect_b32 s100, 32, 48
	s_add_u32 s98, s98, s100
	s_addc_u32 s99, s99, 0
	v_mov_b32_e32 v253, 1
	v_mov_b32_e32 v254, 0
	v_cmp_eq_u32_e32 vcc, 0, v0
	s_and_saveexec_b64 s[100:101], vcc
	s_cbranch_execz .Lmy_cpfx0
	global_atomic_add v254, v254, v253, s[98:99] sc0
.Lmy_cpfx0:
	s_or_b64 exec, exec, s[100:101]
.Lmy_cpf0:
	v_mul_f32_e32 v136, 0x42000000, v192
	v_cvt_pk_fp8_f32 v211, v132, v136 op_sel:[0,0,1]
	v_lshlrev_b64 v[216:217], 9, v[2:3]
	v_lshl_add_u64 v[216:217], v[202:203], 0, v[216:217]
	v_mul_f32_e32 v132, 0x42000000, v137
	global_store_dwordx4 v[216:217], v[208:211], off nt
	v_mul_f32_e32 v136, 0x42000000, v153
	v_mul_f32_e32 v137, 0x42000000, v179
	v_mul_f32_e32 v208, 0x42000000, v133
	v_cvt_pk_fp8_f32 v208, v208, v132
	v_mul_f32_e32 v209, 0x42000000, v149
	v_cvt_pk_fp8_f32 v209, v209, v136
	v_mul_f32_e32 v132, 0x42000000, v141
	v_mul_f32_e32 v133, 0x42000000, v145
	v_cvt_pk_fp8_f32 v208, v132, v133 op_sel:[0,0,1]
	v_mul_f32_e32 v132, 0x42000000, v157
	v_mul_f32_e32 v133, 0x42000000, v161
	v_cvt_pk_fp8_f32 v209, v132, v133 op_sel:[0,0,1]
	v_mul_f32_e32 v210, 0x42000000, v165
	v_mul_f32_e32 v132, 0x42000000, v169
	v_cvt_pk_fp8_f32 v210, v210, v132
	v_mul_f32_e32 v211, 0x42000000, v181
	v_mul_f32_e32 v136, 0x42000000, v185
	v_cvt_pk_fp8_f32 v211, v211, v136
	v_mul_f32_e32 v132, 0x42000000, v173
	v_mul_f32_e32 v133, 0x42000000, v177
	v_cvt_pk_fp8_f32 v210, v132, v133 op_sel:[0,0,1]
	v_mul_f32_e32 v132, 0x42000000, v189
	v_mul_f32_e32 v133, 0x42000000, v193
	v_cvt_pk_fp8_f32 v211, v132, v133 op_sel:[0,0,1]
	v_add_u32_e32 v132, 1, v2
	v_mov_b32_e32 v133, v3
	v_lshlrev_b64 v[132:133], 9, v[132:133]
	v_lshl_add_u64 v[132:133], v[202:203], 0, v[132:133]
	global_store_dwordx4 v[132:133], v[208:211], off nt
	v_mul_f32_e32 v132, 0x42000000, v138
	v_mul_f32_e32 v133, 0x42000000, v146
	v_mul_f32_e32 v208, 0x42000000, v134
	v_cvt_pk_fp8_f32 v208, v208, v132
	v_mul_f32_e32 v209, 0x42000000, v150
	v_mul_f32_e32 v134, 0x42000000, v154
	v_cvt_pk_fp8_f32 v209, v209, v134
	v_mul_f32_e32 v132, 0x42000000, v142
	v_cvt_pk_fp8_f32 v208, v132, v133 op_sel:[0,0,1]
	v_mul_f32_e32 v132, 0x42000000, v158
	v_mul_f32_e32 v133, 0x42000000, v162
	v_cvt_pk_fp8_f32 v209, v132, v133 op_sel:[0,0,1]
	v_mul_f32_e32 v210, 0x42000000, v166
	v_mul_f32_e32 v132, 0x42000000, v170
	v_cvt_pk_fp8_f32 v210, v210, v132
	v_mul_f32_e32 v211, 0x42000000, v182
	v_mul_f32_e32 v134, 0x42000000, v186
	v_cvt_pk_fp8_f32 v211, v211, v134
	v_mul_f32_e32 v132, 0x42000000, v174
	v_mul_f32_e32 v133, 0x42000000, v178
	v_cvt_pk_fp8_f32 v210, v132, v133 op_sel:[0,0,1]
	v_mul_f32_e32 v132, 0x42000000, v190
	v_mul_f32_e32 v133, 0x42000000, v194
	v_cvt_pk_fp8_f32 v211, v132, v133 op_sel:[0,0,1]
	v_add_u32_e32 v132, 2, v2
	v_mov_b32_e32 v133, v3
	v_lshlrev_b64 v[132:133], 9, v[132:133]
	v_lshl_add_u64 v[132:133], v[202:203], 0, v[132:133]
	global_store_dwordx4 v[132:133], v[208:211], off nt
	v_mul_f32_e32 v132, 0x42000000, v135
	v_mul_f32_e32 v133, 0x42000000, v139
	v_cvt_pk_fp8_f32 v132, v132, v133
	v_mul_f32_e32 v133, 0x42000000, v151
	v_mul_f32_e32 v136, 0x42000000, v155
	v_cvt_pk_fp8_f32 v133, v133, v136
	v_mul_f32_e32 v134, 0x42000000, v143
	v_mul_f32_e32 v135, 0x42000000, v147
	v_cvt_pk_fp8_f32 v132, v134, v135 op_sel:[0,0,1]
	v_mul_f32_e32 v134, 0x42000000, v159
	v_mul_f32_e32 v135, 0x42000000, v163
	v_cvt_pk_fp8_f32 v133, v134, v135 op_sel:[0,0,1]
	v_mul_f32_e32 v134, 0x42000000, v167
	v_mul_f32_e32 v135, 0x42000000, v171
	v_cvt_pk_fp8_f32 v134, v134, v135
	v_mul_f32_e32 v135, 0x42000000, v183
	v_mul_f32_e32 v138, 0x42000000, v187
	v_cvt_pk_fp8_f32 v135, v135, v138
	v_mul_f32_e32 v136, 0x42000000, v175
	v_cvt_pk_fp8_f32 v134, v136, v137 op_sel:[0,0,1]
	v_mul_f32_e32 v136, 0x42000000, v191
	v_mul_f32_e32 v137, 0x42000000, v195
	v_cvt_pk_fp8_f32 v135, v136, v137 op_sel:[0,0,1]
	v_add_u32_e32 v136, 3, v2
	v_mov_b32_e32 v137, v3
	v_lshlrev_b64 v[136:137], 9, v[136:137]
	v_lshl_add_u64 v[136:137], v[202:203], 0, v[136:137]
	s_andn2_b64 vcc, exec, s[10:11]
	global_store_dwordx4 v[136:137], v[132:135], off nt
	s_cbranch_vccz .LBB0_432
	s_andn2_b64 vcc, exec, s[86:87]
	s_cbranch_vccnz .LBB0_425
	s_branch .LBB0_433

.LBB0_443:
	s_waitcnt vmcnt(15)
	v_mul_f32_e32 v204, 0x42000000, v132
	s_waitcnt vmcnt(14)
	v_mul_f32_e32 v2, 0x42000000, v136
	v_cvt_pk_fp8_f32 v204, v204, v2
	s_waitcnt vmcnt(1)
	v_mul_f32_e32 v2, 0x42000000, v192
	v_mul_f32_e32 v132, 0x42000000, v172
	v_mul_f32_e32 v205, 0x42000000, v140
	v_cvt_pk_fp8_f32 v204, v2, v132 op_sel:[0,0,1]
	v_mul_f32_e32 v2, 0x42000000, v144
	v_cvt_pk_fp8_f32 v205, v205, v2
	v_mul_f32_e32 v2, 0x42000000, v148
	v_mul_f32_e32 v132, 0x42000000, v152
	v_mul_f32_e32 v206, 0x42000000, v156
	v_cvt_pk_fp8_f32 v205, v2, v132 op_sel:[0,0,1]
	v_mul_f32_e32 v2, 0x42000000, v160
	v_cvt_pk_fp8_f32 v206, v206, v2
	v_mul_f32_e32 v2, 0x42000000, v164
	v_mul_f32_e32 v132, 0x42000000, v184
	v_mul_f32_e32 v207, 0x42000000, v168
	v_cvt_pk_fp8_f32 v206, v2, v132 op_sel:[0,0,1]
	v_mul_f32_e32 v2, 0x42000000, v188
	v_cvt_pk_fp8_f32 v207, v207, v2
	s_and_b32 s31, s34, 0x300
	s_and_b32 s38, s35, 0x60
	v_mul_f32_e32 v2, 0x42000000, v176
	s_waitcnt vmcnt(0)
	s_cmp_lg_u32 s32, 0
	s_cbranch_scc1 .Lmy_cpf1
	s_add_i32 s98, s0, 3
	s_cmp_lt_u32 s98, s1
	s_cbranch_scc1 .Lmy_cpf1
	v_readlane_b32 s32, v255, 20
	v_readlane_b32 s98, v255, 15
	v_readlane_b32 s99, v255, 16
	s_cmp_eq_u32 s32, 1
	s_cselect_b32 s100, 32, 48
	s_add_u32 s98, s98, s100
	s_addc_u32 s99, s99, 0
	v_mov_b32_e32 v253, 1
	v_mov_b32_e32 v254, 0
	v_cmp_eq_u32_e32 vcc, 0, v0
	s_and_saveexec_b64 s[100:101], vcc
	s_cbranch_execz .Lmy_cpfx1
	global_atomic_add v254, v254, v253, s[98:99] sc0

.Lmy_cpf1:
	v_mul_f32_e32 v132, 0x42000000, v180
	s_or_b32 s31, s38, s31
	v_cvt_pk_fp8_f32 v207, v2, v132 op_sel:[0,0,1]
	v_or_b32_e32 v2, s31, v200
	v_lshl_add_u64 v[196:197], s[64:65], 0, v[196:197]
	v_lshlrev_b32_e32 v2, 11, v2
	v_lshl_add_u64 v[196:197], v[196:197], 0, v[2:3]
	v_add_co_u32_e32 v208, vcc, s29, v196
	v_mul_f32_e32 v2, 0x42000000, v137
	s_nop 0
	v_addc_co_u32_e32 v209, vcc, 0, v197, vcc
	v_add_co_u32_e32 v196, vcc, s30, v196
	v_mul_f32_e32 v132, 0x42000000, v173
	s_nop 0
	v_addc_co_u32_e32 v197, vcc, 0, v197, vcc
	global_store_dwordx4 v[196:197], v[204:207], off offset:-4096 nt
	v_mul_f32_e32 v136, 0x42000000, v183
	s_andn2_b64 vcc, exec, s[10:11]
	v_mul_f32_e32 v204, 0x42000000, v133
	v_cvt_pk_fp8_f32 v204, v204, v2
	v_mul_f32_e32 v2, 0x42000000, v193
	v_mul_f32_e32 v205, 0x42000000, v141
	v_mul_f32_e32 v206, 0x42000000, v157
	v_cvt_pk_fp8_f32 v204, v2, v132 op_sel:[0,0,1]
	v_mul_f32_e32 v2, 0x42000000, v145
	v_cvt_pk_fp8_f32 v205, v205, v2
	v_mul_f32_e32 v2, 0x42000000, v149
	v_mul_f32_e32 v132, 0x42000000, v153
	v_mul_f32_e32 v207, 0x42000000, v169
	v_cvt_pk_fp8_f32 v205, v2, v132 op_sel:[0,0,1]
	v_mul_f32_e32 v2, 0x42000000, v161
	v_cvt_pk_fp8_f32 v206, v206, v2
	v_mul_f32_e32 v2, 0x42000000, v165
	v_mul_f32_e32 v132, 0x42000000, v185
	v_mul_f32_e32 v133, 0x42000000, v175
	v_cvt_pk_fp8_f32 v206, v2, v132 op_sel:[0,0,1]
	v_mul_f32_e32 v2, 0x42000000, v189
	v_cvt_pk_fp8_f32 v207, v207, v2
	v_mul_f32_e32 v2, 0x42000000, v177
	v_mul_f32_e32 v132, 0x42000000, v181
	v_cvt_pk_fp8_f32 v207, v2, v132 op_sel:[0,0,1]
	v_mul_f32_e32 v2, 0x42000000, v138
	v_mul_f32_e32 v132, 0x42000000, v174
	global_store_dwordx4 v[208:209], v[204:207], off offset:2048 nt
	s_nop 1
	v_mul_f32_e32 v204, 0x42000000, v134
	v_cvt_pk_fp8_f32 v204, v204, v2
	v_mul_f32_e32 v2, 0x42000000, v194
	v_mul_f32_e32 v205, 0x42000000, v142
	v_mul_f32_e32 v206, 0x42000000, v158
	v_cvt_pk_fp8_f32 v204, v2, v132 op_sel:[0,0,1]
	v_mul_f32_e32 v2, 0x42000000, v146
	v_cvt_pk_fp8_f32 v205, v205, v2
	v_mul_f32_e32 v2, 0x42000000, v150
	v_mul_f32_e32 v132, 0x42000000, v154
	v_mul_f32_e32 v207, 0x42000000, v170
	v_cvt_pk_fp8_f32 v205, v2, v132 op_sel:[0,0,1]
	v_mul_f32_e32 v2, 0x42000000, v162
	v_cvt_pk_fp8_f32 v206, v206, v2
	v_mul_f32_e32 v2, 0x42000000, v166
	v_mul_f32_e32 v132, 0x42000000, v186
	v_mul_f32_e32 v134, 0x42000000, v155
	v_cvt_pk_fp8_f32 v206, v2, v132 op_sel:[0,0,1]
	v_mul_f32_e32 v2, 0x42000000, v190
	v_cvt_pk_fp8_f32 v207, v207, v2
	v_mul_f32_e32 v2, 0x42000000, v178
	v_mul_f32_e32 v132, 0x42000000, v182
	v_cvt_pk_fp8_f32 v207, v2, v132 op_sel:[0,0,1]
	v_mul_f32_e32 v132, 0x42000000, v135
	v_mul_f32_e32 v2, 0x42000000, v139
	v_cvt_pk_fp8_f32 v132, v132, v2
	v_mul_f32_e32 v2, 0x42000000, v195
	v_mul_f32_e32 v135, 0x42000000, v187
	global_store_dwordx4 v[196:197], v[204:207], off nt
	v_cvt_pk_fp8_f32 v132, v2, v133 op_sel:[0,0,1]
	v_mul_f32_e32 v133, 0x42000000, v143
	v_mul_f32_e32 v2, 0x42000000, v147
	v_cvt_pk_fp8_f32 v133, v133, v2
	v_mul_f32_e32 v2, 0x42000000, v151
	v_cvt_pk_fp8_f32 v133, v2, v134 op_sel:[0,0,1]
	v_mul_f32_e32 v134, 0x42000000, v159
	v_mul_f32_e32 v2, 0x42000000, v163
	v_cvt_pk_fp8_f32 v134, v134, v2
	v_mul_f32_e32 v2, 0x42000000, v167
	v_cvt_pk_fp8_f32 v134, v2, v135 op_sel:[0,0,1]
	v_mul_f32_e32 v135, 0x42000000, v171
	v_mul_f32_e32 v2, 0x42000000, v191
	v_cvt_pk_fp8_f32 v135, v135, v2
	v_mul_f32_e32 v2, 0x42000000, v179
	v_cvt_pk_fp8_f32 v135, v2, v136 op_sel:[0,0,1]
	global_store_dwordx4 v[196:197], v[132:135], off offset:2048 nt
	s_cbranch_vccnz .LBB0_445
	s_add_i32 s10, s34, 64
	s_and_b32 s11, s10, 0x7ffffc00
	v_add_u32_e32 v132, s11, v202
	v_ashrrev_i32_e32 v133, 31, v132
	v_lshl_add_u64 v[136:137], s[64:65], 0, v[132:133]
	v_mul_f32_e32 v132, 0x42000000, v64
	v_mul_f32_e32 v2, 0x42000000, v68
	v_cvt_pk_fp8_f32 v132, v132, v2
	v_mul_f32_e32 v2, 0x42000000, v128
	v_mul_f32_e32 v133, 0x42000000, v92
	v_mul_f32_e32 v134, 0x42000000, v80
	v_cvt_pk_fp8_f32 v132, v2, v133 op_sel:[0,0,1]
	v_mul_f32_e32 v133, 0x42000000, v72
	v_mul_f32_e32 v2, 0x42000000, v76
	v_cvt_pk_fp8_f32 v133, v133, v2
	v_mul_f32_e32 v2, 0x42000000, v88
	v_mul_f32_e32 v135, 0x42000000, v124
	s_add_i32 s11, s35, 32
	v_cvt_pk_fp8_f32 v133, v2, v134 op_sel:[0,0,1]
	v_mul_f32_e32 v134, 0x42000000, v84
	v_mul_f32_e32 v2, 0x42000000, v104
	v_cvt_pk_fp8_f32 v134, v134, v2
	v_mul_f32_e32 v2, 0x42000000, v100
	s_and_b32 s10, s10, 0x300
	s_and_b32 s11, s11, 0x60
	v_cvt_pk_fp8_f32 v134, v2, v135 op_sel:[0,0,1]
	v_mul_f32_e32 v135, 0x42000000, v108
	v_mul_f32_e32 v2, 0x42000000, v112
	v_cvt_pk_fp8_f32 v135, v135, v2
	v_mul_f32_e32 v2, 0x42000000, v116
	v_mul_f32_e32 v138, 0x42000000, v120
	s_or_b32 s10, s11, s10
	v_cvt_pk_fp8_f32 v135, v2, v138 op_sel:[0,0,1]
	v_or_b32_e32 v2, s10, v200
	v_lshlrev_b32_e32 v2, 11, v2
	v_lshl_add_u64 v[136:137], v[136:137], 0, v[2:3]
	v_add_co_u32_e32 v138, vcc, s29, v136
	v_mul_f32_e32 v2, 0x42000000, v69
	s_nop 0
	v_addc_co_u32_e32 v139, vcc, 0, v137, vcc
	v_add_co_u32_e32 v136, vcc, s30, v136
	v_mul_f32_e32 v140, 0x42000000, v121
	s_nop 0
	v_addc_co_u32_e32 v137, vcc, 0, v137, vcc
	global_store_dwordx4 v[136:137], v[132:135], off offset:-4096 nt
	s_nop 1
	v_mul_f32_e32 v132, 0x42000000, v65
	v_cvt_pk_fp8_f32 v132, v132, v2
	v_mul_f32_e32 v2, 0x42000000, v129
	v_mul_f32_e32 v133, 0x42000000, v93
	v_mul_f32_e32 v134, 0x42000000, v81
	v_cvt_pk_fp8_f32 v132, v2, v133 op_sel:[0,0,1]
	v_mul_f32_e32 v133, 0x42000000, v73
	v_mul_f32_e32 v2, 0x42000000, v77
	v_cvt_pk_fp8_f32 v133, v133, v2
	v_mul_f32_e32 v2, 0x42000000, v89
	v_mul_f32_e32 v135, 0x42000000, v125
	v_cvt_pk_fp8_f32 v133, v2, v134 op_sel:[0,0,1]
	v_mul_f32_e32 v134, 0x42000000, v85
	v_mul_f32_e32 v2, 0x42000000, v105
	v_cvt_pk_fp8_f32 v134, v134, v2
	v_mul_f32_e32 v2, 0x42000000, v101
	v_cvt_pk_fp8_f32 v134, v2, v135 op_sel:[0,0,1]
	v_mul_f32_e32 v135, 0x42000000, v109
	v_mul_f32_e32 v2, 0x42000000, v113
	v_cvt_pk_fp8_f32 v135, v135, v2
	v_mul_f32_e32 v2, 0x42000000, v117
	v_cvt_pk_fp8_f32 v135, v2, v140 op_sel:[0,0,1]
	v_mul_f32_e32 v2, 0x42000000, v70
	global_store_dwordx4 v[138:139], v[132:135], off offset:2048 nt
	s_nop 1
	v_mul_f32_e32 v132, 0x42000000, v66
	v_cvt_pk_fp8_f32 v132, v132, v2
	v_mul_f32_e32 v2, 0x42000000, v130
	v_mul_f32_e32 v133, 0x42000000, v94
	v_mul_f32_e32 v134, 0x42000000, v82
	v_cvt_pk_fp8_f32 v132, v2, v133 op_sel:[0,0,1]
	v_mul_f32_e32 v133, 0x42000000, v74
	v_mul_f32_e32 v2, 0x42000000, v78
	v_cvt_pk_fp8_f32 v133, v133, v2
	v_mul_f32_e32 v2, 0x42000000, v90
	v_mul_f32_e32 v135, 0x42000000, v126
	v_mul_f32_e32 v138, 0x42000000, v122
	v_cvt_pk_fp8_f32 v133, v2, v134 op_sel:[0,0,1]
	v_mul_f32_e32 v134, 0x42000000, v86
	v_mul_f32_e32 v2, 0x42000000, v106
	v_cvt_pk_fp8_f32 v134, v134, v2
	v_mul_f32_e32 v2, 0x42000000, v102
	v_cvt_pk_fp8_f32 v134, v2, v135 op_sel:[0,0,1]
	v_mul_f32_e32 v135, 0x42000000, v110
	v_mul_f32_e32 v2, 0x42000000, v114
	v_cvt_pk_fp8_f32 v135, v135, v2
	v_mul_f32_e32 v2, 0x42000000, v118
	v_cvt_pk_fp8_f32 v135, v2, v138 op_sel:[0,0,1]
	v_mul_f32_e32 v2, 0x42000000, v71
	v_mul_f32_e32 v138, 0x42000000, v123
	global_store_dwordx4 v[136:137], v[132:135], off nt
	s_nop 1
	v_mul_f32_e32 v132, 0x42000000, v67
	v_cvt_pk_fp8_f32 v132, v132, v2
	v_mul_f32_e32 v2, 0x42000000, v131
	v_mul_f32_e32 v133, 0x42000000, v95
	v_mul_f32_e32 v134, 0x42000000, v83
	v_cvt_pk_fp8_f32 v132, v2, v133 op_sel:[0,0,1]
	v_mul_f32_e32 v133, 0x42000000, v75
	v_mul_f32_e32 v2, 0x42000000, v79
	v_cvt_pk_fp8_f32 v133, v133, v2
	v_mul_f32_e32 v2, 0x42000000, v91
	v_mul_f32_e32 v135, 0x42000000, v127
	v_cvt_pk_fp8_f32 v133, v2, v134 op_sel:[0,0,1]
	v_mul_f32_e32 v134, 0x42000000, v87
	v_mul_f32_e32 v2, 0x42000000, v107
	v_cvt_pk_fp8_f32 v134, v134, v2
	v_mul_f32_e32 v2, 0x42000000, v103
	v_cvt_pk_fp8_f32 v134, v2, v135 op_sel:[0,0,1]
	v_mul_f32_e32 v135, 0x42000000, v111
	v_mul_f32_e32 v2, 0x42000000, v115
	v_cvt_pk_fp8_f32 v135, v135, v2
	v_mul_f32_e32 v2, 0x42000000, v119
	v_cvt_pk_fp8_f32 v135, v2, v138 op_sel:[0,0,1]
	global_store_dwordx4 v[136:137], v[132:135], off offset:2048 nt

.LBB0_456:
	s_waitcnt vmcnt(15)
	v_mul_f32_e32 v204, 0x42000000, v132
	s_waitcnt vmcnt(14)
	v_mul_f32_e32 v2, 0x42000000, v136
	v_cvt_pk_fp8_f32 v204, v204, v2
	s_waitcnt vmcnt(1)
	v_mul_f32_e32 v2, 0x42000000, v192
	v_mul_f32_e32 v132, 0x42000000, v172
	v_mul_f32_e32 v205, 0x42000000, v140
	v_cvt_pk_fp8_f32 v204, v2, v132 op_sel:[0,0,1]
	v_mul_f32_e32 v2, 0x42000000, v144
	v_cvt_pk_fp8_f32 v205, v205, v2
	v_mul_f32_e32 v2, 0x42000000, v148
	v_mul_f32_e32 v132, 0x42000000, v152
	v_mul_f32_e32 v206, 0x42000000, v156
	v_cvt_pk_fp8_f32 v205, v2, v132 op_sel:[0,0,1]
	v_mul_f32_e32 v2, 0x42000000, v160
	v_cvt_pk_fp8_f32 v206, v206, v2
	v_mul_f32_e32 v2, 0x42000000, v164
	v_mul_f32_e32 v132, 0x42000000, v184
	v_mul_f32_e32 v207, 0x42000000, v168
	v_cvt_pk_fp8_f32 v206, v2, v132 op_sel:[0,0,1]
	v_mul_f32_e32 v2, 0x42000000, v188
	v_cvt_pk_fp8_f32 v207, v207, v2
	v_mul_f32_e32 v2, 0x42000000, v176
	s_waitcnt vmcnt(0)
	s_cmp_lg_u32 s32, 0
	s_cbranch_scc1 .Lmy_cpf2
	s_add_i32 s98, s0, 3
	s_cmp_lt_u32 s98, s1
	s_cbranch_scc1 .Lmy_cpf2
	v_readlane_b32 s32, v255, 20
	v_readlane_b32 s98, v255, 15
	v_readlane_b32 s99, v255, 16
	s_cmp_eq_u32 s32, 1
	s_cselect_b32 s100, 32, 48
	s_add_u32 s98, s98, s100
	s_addc_u32 s99, s99, 0
	v_mov_b32_e32 v253, 1
	v_mov_b32_e32 v254, 0
	v_cmp_eq_u32_e32 vcc, 0, v0
	s_and_saveexec_b64 s[100:101], vcc
	s_cbranch_execz .Lmy_cpfx2
	global_atomic_add v254, v254, v253, s[98:99] sc0

.Lmy_cpf2:
	v_mul_f32_e32 v132, 0x42000000, v180
	s_and_b32 s31, s34, 0x300
	s_and_b32 s38, s35, 0x60
	v_cvt_pk_fp8_f32 v207, v2, v132 op_sel:[0,0,1]
	s_or_b32 s31, s38, s31
	v_or_b32_e32 v2, s31, v200
	v_lshl_add_u64 v[196:197], s[64:65], 0, v[196:197]
	v_lshlrev_b32_e32 v2, 11, v2
	v_lshl_add_u64 v[196:197], v[196:197], 0, v[2:3]
	global_store_dwordx4 v[196:197], v[204:207], off nt
	v_mul_f32_e32 v2, 0x42000000, v137
	v_mul_f32_e32 v132, 0x42000000, v173
	v_mul_f32_e32 v204, 0x42000000, v133
	v_cvt_pk_fp8_f32 v204, v204, v2
	v_mul_f32_e32 v2, 0x42000000, v193
	v_mul_f32_e32 v205, 0x42000000, v141
	v_mul_f32_e32 v206, 0x42000000, v157
	v_cvt_pk_fp8_f32 v204, v2, v132 op_sel:[0,0,1]
	v_mul_f32_e32 v2, 0x42000000, v145
	v_cvt_pk_fp8_f32 v205, v205, v2
	v_mul_f32_e32 v2, 0x42000000, v149
	v_mul_f32_e32 v132, 0x42000000, v153
	v_mul_f32_e32 v207, 0x42000000, v169
	v_cvt_pk_fp8_f32 v205, v2, v132 op_sel:[0,0,1]
	v_mul_f32_e32 v2, 0x42000000, v161
	v_cvt_pk_fp8_f32 v206, v206, v2
	v_mul_f32_e32 v2, 0x42000000, v165
	v_mul_f32_e32 v132, 0x42000000, v185
	v_mul_f32_e32 v133, 0x42000000, v175
	v_cvt_pk_fp8_f32 v206, v2, v132 op_sel:[0,0,1]
	v_mul_f32_e32 v2, 0x42000000, v189
	v_cvt_pk_fp8_f32 v207, v207, v2
	v_mul_f32_e32 v2, 0x42000000, v177
	v_mul_f32_e32 v132, 0x42000000, v181
	v_add_co_u32_e32 v136, vcc, s80, v196
	v_cvt_pk_fp8_f32 v207, v2, v132 op_sel:[0,0,1]
	v_mul_f32_e32 v2, 0x42000000, v138
	v_mul_f32_e32 v132, 0x42000000, v174
	v_mul_f32_e32 v138, 0x42000000, v183
	global_store_dwordx4 v[196:197], v[204:207], off offset:2048 nt
	v_addc_co_u32_e32 v137, vcc, 0, v197, vcc
	s_nop 0
	v_mul_f32_e32 v204, 0x42000000, v134
	v_cvt_pk_fp8_f32 v204, v204, v2
	v_mul_f32_e32 v2, 0x42000000, v194
	v_mul_f32_e32 v205, 0x42000000, v142
	v_mul_f32_e32 v206, 0x42000000, v158
	v_cvt_pk_fp8_f32 v204, v2, v132 op_sel:[0,0,1]
	v_mul_f32_e32 v2, 0x42000000, v146
	v_cvt_pk_fp8_f32 v205, v205, v2
	v_mul_f32_e32 v2, 0x42000000, v150
	v_mul_f32_e32 v132, 0x42000000, v154
	v_mul_f32_e32 v207, 0x42000000, v170
	v_cvt_pk_fp8_f32 v205, v2, v132 op_sel:[0,0,1]
	v_mul_f32_e32 v2, 0x42000000, v162
	v_cvt_pk_fp8_f32 v206, v206, v2
	v_mul_f32_e32 v2, 0x42000000, v166
	v_mul_f32_e32 v132, 0x42000000, v186
	v_mul_f32_e32 v134, 0x42000000, v155
	v_cvt_pk_fp8_f32 v206, v2, v132 op_sel:[0,0,1]
	v_mul_f32_e32 v2, 0x42000000, v190
	v_cvt_pk_fp8_f32 v207, v207, v2
	v_mul_f32_e32 v2, 0x42000000, v178
	v_mul_f32_e32 v132, 0x42000000, v182
	s_andn2_b64 vcc, exec, s[10:11]
	v_cvt_pk_fp8_f32 v207, v2, v132 op_sel:[0,0,1]
	v_mul_f32_e32 v132, 0x42000000, v135
	v_mul_f32_e32 v2, 0x42000000, v139
	v_cvt_pk_fp8_f32 v132, v132, v2
	v_mul_f32_e32 v2, 0x42000000, v195
	v_mul_f32_e32 v135, 0x42000000, v187
	global_store_dwordx4 v[136:137], v[204:207], off nt
	v_cvt_pk_fp8_f32 v132, v2, v133 op_sel:[0,0,1]
	v_mul_f32_e32 v133, 0x42000000, v143
	v_mul_f32_e32 v2, 0x42000000, v147
	v_cvt_pk_fp8_f32 v133, v133, v2
	v_mul_f32_e32 v2, 0x42000000, v151
	v_cvt_pk_fp8_f32 v133, v2, v134 op_sel:[0,0,1]
	v_mul_f32_e32 v134, 0x42000000, v159
	v_mul_f32_e32 v2, 0x42000000, v163
	v_cvt_pk_fp8_f32 v134, v134, v2
	v_mul_f32_e32 v2, 0x42000000, v167
	v_cvt_pk_fp8_f32 v134, v2, v135 op_sel:[0,0,1]
	v_mul_f32_e32 v135, 0x42000000, v171
	v_mul_f32_e32 v2, 0x42000000, v191
	v_cvt_pk_fp8_f32 v135, v135, v2
	v_mul_f32_e32 v2, 0x42000000, v179
	v_cvt_pk_fp8_f32 v135, v2, v138 op_sel:[0,0,1]
	global_store_dwordx4 v[136:137], v[132:135], off offset:2048 nt
	s_cbranch_vccnz .LBB0_458
	s_add_i32 s10, s34, 64
	s_and_b32 s11, s10, 0x7ffffc00
	v_add_u32_e32 v132, s11, v202
	v_ashrrev_i32_e32 v133, 31, v132
	v_lshl_add_u64 v[136:137], s[64:65], 0, v[132:133]
	v_mul_f32_e32 v132, 0x42000000, v64
	v_mul_f32_e32 v2, 0x42000000, v68
	v_cvt_pk_fp8_f32 v132, v132, v2
	v_mul_f32_e32 v2, 0x42000000, v128
	v_mul_f32_e32 v133, 0x42000000, v92
	v_mul_f32_e32 v134, 0x42000000, v80
	v_cvt_pk_fp8_f32 v132, v2, v133 op_sel:[0,0,1]
	v_mul_f32_e32 v133, 0x42000000, v72
	v_mul_f32_e32 v2, 0x42000000, v76
	v_cvt_pk_fp8_f32 v133, v133, v2
	v_mul_f32_e32 v2, 0x42000000, v88
	v_mul_f32_e32 v135, 0x42000000, v124
	s_add_i32 s11, s35, 32
	v_cvt_pk_fp8_f32 v133, v2, v134 op_sel:[0,0,1]
	v_mul_f32_e32 v134, 0x42000000, v84
	v_mul_f32_e32 v2, 0x42000000, v104
	v_cvt_pk_fp8_f32 v134, v134, v2
	v_mul_f32_e32 v2, 0x42000000, v100
	v_mul_f32_e32 v138, 0x42000000, v120
	s_and_b32 s10, s10, 0x300
	v_cvt_pk_fp8_f32 v134, v2, v135 op_sel:[0,0,1]
	v_mul_f32_e32 v135, 0x42000000, v108
	v_mul_f32_e32 v2, 0x42000000, v112
	v_cvt_pk_fp8_f32 v135, v135, v2
	v_mul_f32_e32 v2, 0x42000000, v116
	s_and_b32 s11, s11, 0x60
	s_or_b32 s10, s11, s10
	v_cvt_pk_fp8_f32 v135, v2, v138 op_sel:[0,0,1]
	v_or_b32_e32 v2, s10, v200
	v_lshlrev_b32_e32 v2, 11, v2
	v_lshl_add_u64 v[136:137], v[136:137], 0, v[2:3]
	global_store_dwordx4 v[136:137], v[132:135], off nt
	v_mul_f32_e32 v2, 0x42000000, v69
	v_mul_f32_e32 v138, 0x42000000, v121
	v_mul_f32_e32 v132, 0x42000000, v65
	v_cvt_pk_fp8_f32 v132, v132, v2
	v_mul_f32_e32 v2, 0x42000000, v129
	v_mul_f32_e32 v133, 0x42000000, v93
	v_mul_f32_e32 v134, 0x42000000, v81
	v_cvt_pk_fp8_f32 v132, v2, v133 op_sel:[0,0,1]
	v_mul_f32_e32 v133, 0x42000000, v73
	v_mul_f32_e32 v2, 0x42000000, v77
	v_cvt_pk_fp8_f32 v133, v133, v2
	v_mul_f32_e32 v2, 0x42000000, v89
	v_mul_f32_e32 v135, 0x42000000, v125
	v_cvt_pk_fp8_f32 v133, v2, v134 op_sel:[0,0,1]
	v_mul_f32_e32 v134, 0x42000000, v85
	v_mul_f32_e32 v2, 0x42000000, v105
	v_cvt_pk_fp8_f32 v134, v134, v2
	v_mul_f32_e32 v2, 0x42000000, v101
	v_cvt_pk_fp8_f32 v134, v2, v135 op_sel:[0,0,1]
	v_mul_f32_e32 v135, 0x42000000, v109
	v_mul_f32_e32 v2, 0x42000000, v113
	v_cvt_pk_fp8_f32 v135, v135, v2
	v_mul_f32_e32 v2, 0x42000000, v117
	v_cvt_pk_fp8_f32 v135, v2, v138 op_sel:[0,0,1]
	v_mul_f32_e32 v2, 0x42000000, v70
	v_mul_f32_e32 v138, 0x42000000, v122
	global_store_dwordx4 v[136:137], v[132:135], off offset:2048 nt
	v_add_co_u32_e32 v136, vcc, s80, v136
	s_nop 0
	v_mul_f32_e32 v132, 0x42000000, v66
	v_cvt_pk_fp8_f32 v132, v132, v2
	v_mul_f32_e32 v2, 0x42000000, v130
	v_mul_f32_e32 v133, 0x42000000, v94
	v_mul_f32_e32 v134, 0x42000000, v82
	v_cvt_pk_fp8_f32 v132, v2, v133 op_sel:[0,0,1]
	v_mul_f32_e32 v133, 0x42000000, v74
	v_mul_f32_e32 v2, 0x42000000, v78
	v_cvt_pk_fp8_f32 v133, v133, v2
	v_mul_f32_e32 v2, 0x42000000, v90
	v_mul_f32_e32 v135, 0x42000000, v126
	v_addc_co_u32_e32 v137, vcc, 0, v137, vcc
	v_cvt_pk_fp8_f32 v133, v2, v134 op_sel:[0,0,1]
	v_mul_f32_e32 v134, 0x42000000, v86
	v_mul_f32_e32 v2, 0x42000000, v106
	v_cvt_pk_fp8_f32 v134, v134, v2
	v_mul_f32_e32 v2, 0x42000000, v102
	v_cvt_pk_fp8_f32 v134, v2, v135 op_sel:[0,0,1]
	v_mul_f32_e32 v135, 0x42000000, v110
	v_mul_f32_e32 v2, 0x42000000, v114
	v_cvt_pk_fp8_f32 v135, v135, v2
	v_mul_f32_e32 v2, 0x42000000, v118
	v_cvt_pk_fp8_f32 v135, v2, v138 op_sel:[0,0,1]
	v_mul_f32_e32 v2, 0x42000000, v71
	v_mul_f32_e32 v138, 0x42000000, v123
	global_store_dwordx4 v[136:137], v[132:135], off nt
	s_nop 1
	v_mul_f32_e32 v132, 0x42000000, v67
	v_cvt_pk_fp8_f32 v132, v132, v2
	v_mul_f32_e32 v2, 0x42000000, v131
	v_mul_f32_e32 v133, 0x42000000, v95
	v_mul_f32_e32 v134, 0x42000000, v83
	v_cvt_pk_fp8_f32 v132, v2, v133 op_sel:[0,0,1]
	v_mul_f32_e32 v133, 0x42000000, v75
	v_mul_f32_e32 v2, 0x42000000, v79
	v_cvt_pk_fp8_f32 v133, v133, v2
	v_mul_f32_e32 v2, 0x42000000, v91
	v_mul_f32_e32 v135, 0x42000000, v127
	v_cvt_pk_fp8_f32 v133, v2, v134 op_sel:[0,0,1]
	v_mul_f32_e32 v134, 0x42000000, v87
	v_mul_f32_e32 v2, 0x42000000, v107
	v_cvt_pk_fp8_f32 v134, v134, v2
	v_mul_f32_e32 v2, 0x42000000, v103
	v_cvt_pk_fp8_f32 v134, v2, v135 op_sel:[0,0,1]
	v_mul_f32_e32 v135, 0x42000000, v111
	v_mul_f32_e32 v2, 0x42000000, v115
	v_cvt_pk_fp8_f32 v135, v135, v2
	v_mul_f32_e32 v2, 0x42000000, v119
	v_cvt_pk_fp8_f32 v135, v2, v138 op_sel:[0,0,1]
	global_store_dwordx4 v[136:137], v[132:135], off offset:2048 nt

.LBB0_469:
	s_waitcnt vmcnt(15)
	v_mul_f32_e32 v206, 0x42000000, v132
	s_waitcnt vmcnt(14)
	v_mul_f32_e32 v2, 0x42000000, v136
	v_cvt_pk_fp8_f32 v206, v206, v2
	s_waitcnt vmcnt(13)
	v_mul_f32_e32 v2, 0x42000000, v140
	s_waitcnt vmcnt(12)
	v_mul_f32_e32 v132, 0x42000000, v144
	s_waitcnt vmcnt(11)
	v_mul_f32_e32 v207, 0x42000000, v148
	v_cvt_pk_fp8_f32 v206, v2, v132 op_sel:[0,0,1]
	s_waitcnt vmcnt(10)
	v_mul_f32_e32 v2, 0x42000000, v152
	v_cvt_pk_fp8_f32 v207, v207, v2
	s_waitcnt vmcnt(9)
	v_mul_f32_e32 v2, 0x42000000, v156
	s_waitcnt vmcnt(8)
	v_mul_f32_e32 v132, 0x42000000, v160
	s_waitcnt vmcnt(7)
	v_mul_f32_e32 v208, 0x42000000, v164
	v_cvt_pk_fp8_f32 v207, v2, v132 op_sel:[0,0,1]
	s_waitcnt vmcnt(6)
	v_mul_f32_e32 v2, 0x42000000, v168
	v_cvt_pk_fp8_f32 v208, v208, v2
	s_waitcnt vmcnt(5)
	v_mul_f32_e32 v2, 0x42000000, v172
	s_waitcnt vmcnt(4)
	v_mul_f32_e32 v132, 0x42000000, v176
	s_waitcnt vmcnt(3)
	v_mul_f32_e32 v209, 0x42000000, v180
	v_cvt_pk_fp8_f32 v208, v2, v132 op_sel:[0,0,1]
	s_waitcnt vmcnt(2)
	v_mul_f32_e32 v2, 0x42000000, v184
	v_cvt_pk_fp8_f32 v209, v209, v2
	s_lshl_b64 s[38:39], s[40:41], 20
	s_waitcnt vmcnt(1)
	v_mul_f32_e32 v2, 0x42000000, v188
	s_waitcnt vmcnt(0)
	s_cmp_lg_u32 s32, 0
	s_cbranch_scc1 .Lmy_cpf3
	s_add_i32 s98, s0, 3
	s_cmp_lt_u32 s98, s1
	s_cbranch_scc1 .Lmy_cpf3
	v_readlane_b32 s32, v255, 20
	v_readlane_b32 s98, v255, 15
	v_readlane_b32 s99, v255, 16
	s_cmp_eq_u32 s32, 1
	s_cselect_b32 s100, 32, 48
	s_add_u32 s98, s98, s100
	s_addc_u32 s99, s99, 0
	v_mov_b32_e32 v253, 1
	v_mov_b32_e32 v254, 0
	v_cmp_eq_u32_e32 vcc, 0, v0
	s_and_saveexec_b64 s[100:101], vcc
	s_cbranch_execz .Lmy_cpfx3
	global_atomic_add v254, v254, v253, s[98:99] sc0

.Lmy_cpf3:
	v_mul_f32_e32 v132, 0x42000000, v192
	v_lshl_add_u64 v[210:211], v[202:203], 0, s[38:39]
	v_cvt_pk_fp8_f32 v209, v2, v132 op_sel:[0,0,1]
	v_lshlrev_b32_e32 v2, 9, v204
	v_lshl_add_u64 v[210:211], v[210:211], 0, v[2:3]
	v_mul_f32_e32 v204, 0x42000000, v133
	v_mul_f32_e32 v2, 0x42000000, v137
	v_cvt_pk_fp8_f32 v204, v204, v2
	v_mul_f32_e32 v2, 0x42000000, v141
	v_mul_f32_e32 v132, 0x42000000, v145
	v_mul_f32_e32 v205, 0x42000000, v149
	v_cvt_pk_fp8_f32 v204, v2, v132 op_sel:[0,0,1]
	v_mul_f32_e32 v2, 0x42000000, v153
	v_cvt_pk_fp8_f32 v205, v205, v2
	v_mul_f32_e32 v2, 0x42000000, v157
	v_mul_f32_e32 v132, 0x42000000, v161
	global_store_dwordx4 v[210:211], v[206:209], off nt
	v_cvt_pk_fp8_f32 v205, v2, v132 op_sel:[0,0,1]
	v_mul_f32_e32 v2, 0x42000000, v169
	v_mul_f32_e32 v206, 0x42000000, v165
	v_cvt_pk_fp8_f32 v206, v206, v2
	v_mul_f32_e32 v2, 0x42000000, v173
	v_mul_f32_e32 v132, 0x42000000, v177
	v_mul_f32_e32 v207, 0x42000000, v181
	v_cvt_pk_fp8_f32 v206, v2, v132 op_sel:[0,0,1]
	v_mul_f32_e32 v2, 0x42000000, v185
	v_cvt_pk_fp8_f32 v207, v207, v2
	v_mul_f32_e32 v2, 0x42000000, v189
	v_mul_f32_e32 v132, 0x42000000, v193
	v_mul_f32_e32 v133, 0x42000000, v147
	v_cvt_pk_fp8_f32 v207, v2, v132 op_sel:[0,0,1]
	v_mul_f32_e32 v2, 0x42000000, v138
	v_mul_f32_e32 v132, 0x42000000, v146
	v_mul_f32_e32 v136, 0x42000000, v195
	global_store_dwordx4 v[210:211], v[204:207], off offset:512 nt
	s_andn2_b64 vcc, exec, s[10:11]
	s_nop 0
	v_mul_f32_e32 v204, 0x42000000, v134
	v_cvt_pk_fp8_f32 v204, v204, v2
	v_mul_f32_e32 v2, 0x42000000, v142
	v_mul_f32_e32 v205, 0x42000000, v150
	v_mul_f32_e32 v206, 0x42000000, v166
	v_cvt_pk_fp8_f32 v204, v2, v132 op_sel:[0,0,1]
	v_mul_f32_e32 v2, 0x42000000, v154
	v_cvt_pk_fp8_f32 v205, v205, v2
	v_mul_f32_e32 v2, 0x42000000, v158
	v_mul_f32_e32 v132, 0x42000000, v162
	v_mul_f32_e32 v207, 0x42000000, v182
	v_cvt_pk_fp8_f32 v205, v2, v132 op_sel:[0,0,1]
	v_mul_f32_e32 v2, 0x42000000, v170
	v_cvt_pk_fp8_f32 v206, v206, v2
	v_mul_f32_e32 v2, 0x42000000, v174
	v_mul_f32_e32 v132, 0x42000000, v178
	v_mul_f32_e32 v134, 0x42000000, v163
	v_cvt_pk_fp8_f32 v206, v2, v132 op_sel:[0,0,1]
	v_mul_f32_e32 v2, 0x42000000, v186
	v_cvt_pk_fp8_f32 v207, v207, v2
	v_mul_f32_e32 v2, 0x42000000, v190
	v_mul_f32_e32 v132, 0x42000000, v194
	v_cvt_pk_fp8_f32 v207, v2, v132 op_sel:[0,0,1]
	v_mul_f32_e32 v132, 0x42000000, v135
	v_mul_f32_e32 v2, 0x42000000, v139
	v_cvt_pk_fp8_f32 v132, v132, v2
	v_mul_f32_e32 v2, 0x42000000, v143
	v_mul_f32_e32 v135, 0x42000000, v179
	global_store_dwordx4 v[210:211], v[204:207], off offset:1024 nt
	v_cvt_pk_fp8_f32 v132, v2, v133 op_sel:[0,0,1]
	v_mul_f32_e32 v133, 0x42000000, v151
	v_mul_f32_e32 v2, 0x42000000, v155
	v_cvt_pk_fp8_f32 v133, v133, v2
	v_mul_f32_e32 v2, 0x42000000, v159
	v_cvt_pk_fp8_f32 v133, v2, v134 op_sel:[0,0,1]
	v_mul_f32_e32 v134, 0x42000000, v167
	v_mul_f32_e32 v2, 0x42000000, v171
	v_cvt_pk_fp8_f32 v134, v134, v2
	v_mul_f32_e32 v2, 0x42000000, v175
	v_cvt_pk_fp8_f32 v134, v2, v135 op_sel:[0,0,1]
	v_mul_f32_e32 v135, 0x42000000, v183
	v_mul_f32_e32 v2, 0x42000000, v187
	v_cvt_pk_fp8_f32 v135, v135, v2
	v_mul_f32_e32 v2, 0x42000000, v191
	v_cvt_pk_fp8_f32 v135, v2, v136 op_sel:[0,0,1]
	global_store_dwordx4 v[210:211], v[132:135], off offset:1536 nt
	s_cbranch_vccz .LBB0_471
	s_andn2_b64 vcc, exec, s[86:87]
	s_cbranch_vccnz .LBB0_464
	s_branch .LBB0_472

.LBB0_482:
	s_waitcnt vmcnt(15)
	v_mul_f32_e32 v204, 0x42000000, v132
	s_waitcnt vmcnt(14)
	v_mul_f32_e32 v2, 0x42000000, v136
	v_cvt_pk_fp8_f32 v204, v204, v2
	s_waitcnt vmcnt(1)
	v_mul_f32_e32 v2, 0x42000000, v192
	v_mul_f32_e32 v132, 0x42000000, v172
	v_mul_f32_e32 v205, 0x42000000, v140
	v_cvt_pk_fp8_f32 v204, v2, v132 op_sel:[0,0,1]
	v_mul_f32_e32 v2, 0x42000000, v144
	v_cvt_pk_fp8_f32 v205, v205, v2
	v_mul_f32_e32 v2, 0x42000000, v148
	v_mul_f32_e32 v132, 0x42000000, v152
	v_mul_f32_e32 v206, 0x42000000, v156
	v_cvt_pk_fp8_f32 v205, v2, v132 op_sel:[0,0,1]
	v_mul_f32_e32 v2, 0x42000000, v160
	v_cvt_pk_fp8_f32 v206, v206, v2
	v_mul_f32_e32 v2, 0x42000000, v164
	v_mul_f32_e32 v132, 0x42000000, v184
	v_mul_f32_e32 v207, 0x42000000, v168
	v_cvt_pk_fp8_f32 v206, v2, v132 op_sel:[0,0,1]
	v_mul_f32_e32 v2, 0x42000000, v188
	s_lshl_b64 s[44:45], s[40:41], 21
	v_cvt_pk_fp8_f32 v207, v207, v2
	s_add_u32 s44, s20, s44
	s_addc_u32 s45, s21, s45
	s_and_b32 s39, s34, 0x300
	s_and_b32 s40, s35, 0x60
	v_mul_f32_e32 v2, 0x42000000, v176
	s_waitcnt vmcnt(0)
	s_cmp_lg_u32 s32, 0
	s_cbranch_scc1 .Lmy_cpf4
	s_add_i32 s98, s0, 3
	s_cmp_lt_u32 s98, s1
	s_cbranch_scc1 .Lmy_cpf4
	v_readlane_b32 s32, v255, 20
	v_readlane_b32 s98, v255, 15
	v_readlane_b32 s99, v255, 16
	s_cmp_eq_u32 s32, 1
	s_cselect_b32 s100, 32, 48
	s_add_u32 s98, s98, s100
	s_addc_u32 s99, s99, 0
	v_mov_b32_e32 v253, 1
	v_mov_b32_e32 v254, 0
	v_cmp_eq_u32_e32 vcc, 0, v0
	s_and_saveexec_b64 s[100:101], vcc
	s_cbranch_execz .Lmy_cpfx4
	global_atomic_add v254, v254, v253, s[98:99] sc0

.Lmy_cpf4:
	v_mul_f32_e32 v132, 0x42000000, v180
	s_or_b32 s39, s40, s39
	v_cvt_pk_fp8_f32 v207, v2, v132 op_sel:[0,0,1]
	v_or_b32_e32 v2, s39, v200
	v_lshl_add_u64 v[196:197], s[44:45], 0, v[196:197]
	v_lshlrev_b32_e32 v2, 11, v2
	v_lshl_add_u64 v[196:197], v[196:197], 0, v[2:3]
	v_add_co_u32_e32 v208, vcc, s29, v196
	v_mul_f32_e32 v2, 0x42000000, v137
	s_nop 0
	v_addc_co_u32_e32 v209, vcc, 0, v197, vcc
	v_add_co_u32_e32 v196, vcc, s30, v196
	v_mul_f32_e32 v132, 0x42000000, v173
	s_nop 0
	v_addc_co_u32_e32 v197, vcc, 0, v197, vcc
	global_store_dwordx4 v[196:197], v[204:207], off offset:-4096 nt
	v_mul_f32_e32 v136, 0x42000000, v183
	s_andn2_b64 vcc, exec, s[10:11]
	v_mul_f32_e32 v204, 0x42000000, v133
	v_cvt_pk_fp8_f32 v204, v204, v2
	v_mul_f32_e32 v2, 0x42000000, v193
	v_mul_f32_e32 v205, 0x42000000, v141
	v_mul_f32_e32 v206, 0x42000000, v157
	v_cvt_pk_fp8_f32 v204, v2, v132 op_sel:[0,0,1]
	v_mul_f32_e32 v2, 0x42000000, v145
	v_cvt_pk_fp8_f32 v205, v205, v2
	v_mul_f32_e32 v2, 0x42000000, v149
	v_mul_f32_e32 v132, 0x42000000, v153
	v_mul_f32_e32 v207, 0x42000000, v169
	v_cvt_pk_fp8_f32 v205, v2, v132 op_sel:[0,0,1]
	v_mul_f32_e32 v2, 0x42000000, v161
	v_cvt_pk_fp8_f32 v206, v206, v2
	v_mul_f32_e32 v2, 0x42000000, v165
	v_mul_f32_e32 v132, 0x42000000, v185
	v_mul_f32_e32 v133, 0x42000000, v175
	v_cvt_pk_fp8_f32 v206, v2, v132 op_sel:[0,0,1]
	v_mul_f32_e32 v2, 0x42000000, v189
	v_cvt_pk_fp8_f32 v207, v207, v2
	v_mul_f32_e32 v2, 0x42000000, v177
	v_mul_f32_e32 v132, 0x42000000, v181
	v_cvt_pk_fp8_f32 v207, v2, v132 op_sel:[0,0,1]
	v_mul_f32_e32 v2, 0x42000000, v138
	v_mul_f32_e32 v132, 0x42000000, v174
	global_store_dwordx4 v[208:209], v[204:207], off offset:2048 nt
	s_nop 1
	v_mul_f32_e32 v204, 0x42000000, v134
	v_cvt_pk_fp8_f32 v204, v204, v2
	v_mul_f32_e32 v2, 0x42000000, v194
	v_mul_f32_e32 v205, 0x42000000, v142
	v_mul_f32_e32 v206, 0x42000000, v158
	v_cvt_pk_fp8_f32 v204, v2, v132 op_sel:[0,0,1]
	v_mul_f32_e32 v2, 0x42000000, v146
	v_cvt_pk_fp8_f32 v205, v205, v2
	v_mul_f32_e32 v2, 0x42000000, v150
	v_mul_f32_e32 v132, 0x42000000, v154
	v_mul_f32_e32 v207, 0x42000000, v170
	v_cvt_pk_fp8_f32 v205, v2, v132 op_sel:[0,0,1]
	v_mul_f32_e32 v2, 0x42000000, v162
	v_cvt_pk_fp8_f32 v206, v206, v2
	v_mul_f32_e32 v2, 0x42000000, v166
	v_mul_f32_e32 v132, 0x42000000, v186
	v_mul_f32_e32 v134, 0x42000000, v155
	v_cvt_pk_fp8_f32 v206, v2, v132 op_sel:[0,0,1]
	v_mul_f32_e32 v2, 0x42000000, v190
	v_cvt_pk_fp8_f32 v207, v207, v2
	v_mul_f32_e32 v2, 0x42000000, v178
	v_mul_f32_e32 v132, 0x42000000, v182
	v_cvt_pk_fp8_f32 v207, v2, v132 op_sel:[0,0,1]
	v_mul_f32_e32 v132, 0x42000000, v135
	v_mul_f32_e32 v2, 0x42000000, v139
	v_cvt_pk_fp8_f32 v132, v132, v2
	v_mul_f32_e32 v2, 0x42000000, v195
	v_mul_f32_e32 v135, 0x42000000, v187
	global_store_dwordx4 v[196:197], v[204:207], off nt
	v_cvt_pk_fp8_f32 v132, v2, v133 op_sel:[0,0,1]
	v_mul_f32_e32 v133, 0x42000000, v143
	v_mul_f32_e32 v2, 0x42000000, v147
	v_cvt_pk_fp8_f32 v133, v133, v2
	v_mul_f32_e32 v2, 0x42000000, v151
	v_cvt_pk_fp8_f32 v133, v2, v134 op_sel:[0,0,1]
	v_mul_f32_e32 v134, 0x42000000, v159
	v_mul_f32_e32 v2, 0x42000000, v163
	v_cvt_pk_fp8_f32 v134, v134, v2
	v_mul_f32_e32 v2, 0x42000000, v167
	v_cvt_pk_fp8_f32 v134, v2, v135 op_sel:[0,0,1]
	v_mul_f32_e32 v135, 0x42000000, v171
	v_mul_f32_e32 v2, 0x42000000, v191
	v_cvt_pk_fp8_f32 v135, v135, v2
	v_mul_f32_e32 v2, 0x42000000, v179
	v_cvt_pk_fp8_f32 v135, v2, v136 op_sel:[0,0,1]
	global_store_dwordx4 v[196:197], v[132:135], off offset:2048 nt
	s_cbranch_vccnz .LBB0_484
	s_lshr_b32 s40, s31, 5
	s_add_i32 s31, s34, 64
	s_and_b32 s10, s31, 0x400
	v_add_u32_e32 v132, s10, v202
	s_add_i32 s39, s35, 32
	s_lshl_b64 s[10:11], s[40:41], 21
	s_add_u32 s10, s20, s10
	s_addc_u32 s11, s21, s11
	v_ashrrev_i32_e32 v133, 31, v132
	v_lshl_add_u64 v[136:137], s[10:11], 0, v[132:133]
	v_mul_f32_e32 v132, 0x42000000, v64
	v_mul_f32_e32 v2, 0x42000000, v68
	v_cvt_pk_fp8_f32 v132, v132, v2
	v_mul_f32_e32 v2, 0x42000000, v128
	v_mul_f32_e32 v133, 0x42000000, v92
	v_mul_f32_e32 v134, 0x42000000, v80
	v_cvt_pk_fp8_f32 v132, v2, v133 op_sel:[0,0,1]
	v_mul_f32_e32 v133, 0x42000000, v72
	v_mul_f32_e32 v2, 0x42000000, v76
	v_cvt_pk_fp8_f32 v133, v133, v2
	v_mul_f32_e32 v2, 0x42000000, v88
	v_mul_f32_e32 v135, 0x42000000, v124
	s_and_b32 s10, s31, 0x300
	v_cvt_pk_fp8_f32 v133, v2, v134 op_sel:[0,0,1]
	v_mul_f32_e32 v134, 0x42000000, v84
	v_mul_f32_e32 v2, 0x42000000, v104
	v_cvt_pk_fp8_f32 v134, v134, v2
	v_mul_f32_e32 v2, 0x42000000, v100
	s_and_b32 s11, s39, 0x60
	v_mul_f32_e32 v138, 0x42000000, v120
	v_cvt_pk_fp8_f32 v134, v2, v135 op_sel:[0,0,1]
	v_mul_f32_e32 v135, 0x42000000, v108
	v_mul_f32_e32 v2, 0x42000000, v112
	v_cvt_pk_fp8_f32 v135, v135, v2
	v_mul_f32_e32 v2, 0x42000000, v116
	s_or_b32 s10, s11, s10
	v_mul_f32_e32 v140, 0x42000000, v121
	v_cvt_pk_fp8_f32 v135, v2, v138 op_sel:[0,0,1]
	v_or_b32_e32 v2, s10, v200
	v_lshlrev_b32_e32 v2, 11, v2
	v_lshl_add_u64 v[136:137], v[136:137], 0, v[2:3]
	v_add_co_u32_e32 v138, vcc, s29, v136
	v_mul_f32_e32 v2, 0x42000000, v69
	s_nop 0
	v_addc_co_u32_e32 v139, vcc, 0, v137, vcc
	v_add_co_u32_e32 v136, vcc, s30, v136
	s_nop 1
	v_addc_co_u32_e32 v137, vcc, 0, v137, vcc
	global_store_dwordx4 v[136:137], v[132:135], off offset:-4096 nt
	s_nop 1
	v_mul_f32_e32 v132, 0x42000000, v65
	v_cvt_pk_fp8_f32 v132, v132, v2
	v_mul_f32_e32 v2, 0x42000000, v129
	v_mul_f32_e32 v133, 0x42000000, v93
	v_mul_f32_e32 v134, 0x42000000, v81
	v_cvt_pk_fp8_f32 v132, v2, v133 op_sel:[0,0,1]
	v_mul_f32_e32 v133, 0x42000000, v73
	v_mul_f32_e32 v2, 0x42000000, v77
	v_cvt_pk_fp8_f32 v133, v133, v2
	v_mul_f32_e32 v2, 0x42000000, v89
	v_mul_f32_e32 v135, 0x42000000, v125
	v_cvt_pk_fp8_f32 v133, v2, v134 op_sel:[0,0,1]
	v_mul_f32_e32 v134, 0x42000000, v85
	v_mul_f32_e32 v2, 0x42000000, v105
	v_cvt_pk_fp8_f32 v134, v134, v2
	v_mul_f32_e32 v2, 0x42000000, v101
	v_cvt_pk_fp8_f32 v134, v2, v135 op_sel:[0,0,1]
	v_mul_f32_e32 v135, 0x42000000, v109
	v_mul_f32_e32 v2, 0x42000000, v113
	v_cvt_pk_fp8_f32 v135, v135, v2
	v_mul_f32_e32 v2, 0x42000000, v117
	v_cvt_pk_fp8_f32 v135, v2, v140 op_sel:[0,0,1]
	v_mul_f32_e32 v2, 0x42000000, v70
	global_store_dwordx4 v[138:139], v[132:135], off offset:2048 nt
	s_nop 1
	v_mul_f32_e32 v132, 0x42000000, v66
	v_cvt_pk_fp8_f32 v132, v132, v2
	v_mul_f32_e32 v2, 0x42000000, v130
	v_mul_f32_e32 v133, 0x42000000, v94
	v_mul_f32_e32 v134, 0x42000000, v82
	v_cvt_pk_fp8_f32 v132, v2, v133 op_sel:[0,0,1]
	v_mul_f32_e32 v133, 0x42000000, v74
	v_mul_f32_e32 v2, 0x42000000, v78
	v_cvt_pk_fp8_f32 v133, v133, v2
	v_mul_f32_e32 v2, 0x42000000, v90
	v_mul_f32_e32 v135, 0x42000000, v126
	v_mul_f32_e32 v138, 0x42000000, v122
	v_cvt_pk_fp8_f32 v133, v2, v134 op_sel:[0,0,1]
	v_mul_f32_e32 v134, 0x42000000, v86
	v_mul_f32_e32 v2, 0x42000000, v106
	v_cvt_pk_fp8_f32 v134, v134, v2
	v_mul_f32_e32 v2, 0x42000000, v102
	v_cvt_pk_fp8_f32 v134, v2, v135 op_sel:[0,0,1]
	v_mul_f32_e32 v135, 0x42000000, v110
	v_mul_f32_e32 v2, 0x42000000, v114
	v_cvt_pk_fp8_f32 v135, v135, v2
	v_mul_f32_e32 v2, 0x42000000, v118
	v_cvt_pk_fp8_f32 v135, v2, v138 op_sel:[0,0,1]
	v_mul_f32_e32 v2, 0x42000000, v71
	v_mul_f32_e32 v138, 0x42000000, v123
	global_store_dwordx4 v[136:137], v[132:135], off nt
	s_nop 1
	v_mul_f32_e32 v132, 0x42000000, v67
	v_cvt_pk_fp8_f32 v132, v132, v2
	v_mul_f32_e32 v2, 0x42000000, v131
	v_mul_f32_e32 v133, 0x42000000, v95
	v_mul_f32_e32 v134, 0x42000000, v83
	v_cvt_pk_fp8_f32 v132, v2, v133 op_sel:[0,0,1]
	v_mul_f32_e32 v133, 0x42000000, v75
	v_mul_f32_e32 v2, 0x42000000, v79
	v_cvt_pk_fp8_f32 v133, v133, v2
	v_mul_f32_e32 v2, 0x42000000, v91
	v_mul_f32_e32 v135, 0x42000000, v127
	v_cvt_pk_fp8_f32 v133, v2, v134 op_sel:[0,0,1]
	v_mul_f32_e32 v134, 0x42000000, v87
	v_mul_f32_e32 v2, 0x42000000, v107
	v_cvt_pk_fp8_f32 v134, v134, v2
	v_mul_f32_e32 v2, 0x42000000, v103
	v_cvt_pk_fp8_f32 v134, v2, v135 op_sel:[0,0,1]
	v_mul_f32_e32 v135, 0x42000000, v111
	v_mul_f32_e32 v2, 0x42000000, v115
	v_cvt_pk_fp8_f32 v135, v135, v2
	v_mul_f32_e32 v2, 0x42000000, v119
	v_cvt_pk_fp8_f32 v135, v2, v138 op_sel:[0,0,1]
	global_store_dwordx4 v[136:137], v[132:135], off offset:2048 nt

.LBB0_495:
	s_waitcnt vmcnt(15)
	v_mul_f32_e32 v202, 0x42000000, v132
	s_waitcnt vmcnt(14)
	v_mul_f32_e32 v132, 0x42000000, v136
	v_cvt_pk_fp8_f32 v202, v202, v132
	s_waitcnt vmcnt(13)
	v_mul_f32_e32 v203, 0x42000000, v140
	s_waitcnt vmcnt(12)
	v_mul_f32_e32 v140, 0x42000000, v144
	v_cvt_pk_fp8_f32 v203, v203, v140
	s_waitcnt vmcnt(1)
	v_mul_f32_e32 v132, 0x42000000, v192
	v_mul_f32_e32 v136, 0x42000000, v152
	v_cvt_pk_fp8_f32 v202, v132, v136 op_sel:[0,0,1]
	v_mul_f32_e32 v132, 0x42000000, v148
	v_mul_f32_e32 v136, 0x42000000, v156
	v_cvt_pk_fp8_f32 v203, v132, v136 op_sel:[0,0,1]
	v_mul_f32_e32 v204, 0x42000000, v160
	v_mul_f32_e32 v132, 0x42000000, v164
	s_lshl_b64 s[44:45], s[86:87], 21
	v_cvt_pk_fp8_f32 v204, v204, v132
	v_mul_f32_e32 v205, 0x42000000, v176
	v_mul_f32_e32 v140, 0x42000000, v184
	s_add_u32 s44, s20, s44
	v_cvt_pk_fp8_f32 v205, v205, v140
	s_addc_u32 s45, s21, s45
	s_lshl_b32 s35, s35, 6
	v_mul_f32_e32 v132, 0x42000000, v168
	v_mul_f32_e32 v136, 0x42000000, v172
	s_and_b32 s35, s35, 0xffffff00
	s_and_b32 s34, s34, 0x60
	v_cvt_pk_fp8_f32 v204, v132, v136 op_sel:[0,0,1]
	v_mul_f32_e32 v132, 0x42000000, v180
	s_waitcnt vmcnt(0)
	s_cmp_lg_u32 s32, 0
	s_cbranch_scc1 .Lmy_cpf5
	s_add_i32 s98, s0, 3
	s_cmp_lt_i32 s98, s1
	s_cbranch_scc1 .Lmy_cpf5
	v_readlane_b32 s32, v255, 20
	v_readlane_b32 s98, v255, 15
	v_readlane_b32 s99, v255, 16
	s_cmp_eq_u32 s32, 1
	s_cselect_b32 s100, 32, 48
	s_add_u32 s98, s98, s100
	s_addc_u32 s99, s99, 0
	v_mov_b32_e32 v253, 1
	v_mov_b32_e32 v254, 0
	v_cmp_eq_u32_e32 vcc, 0, v0
	s_and_saveexec_b64 s[100:101], vcc
	s_cbranch_execz .Lmy_cpfx5
	global_atomic_add v254, v254, v253, s[98:99] sc0

.Lmy_cpf5:
	v_mul_f32_e32 v136, 0x42000000, v188
	s_or_b32 s34, s35, s34
	v_cvt_pk_fp8_f32 v205, v132, v136 op_sel:[0,0,1]
	v_or_b32_e32 v206, s34, v2
	v_ashrrev_i32_e32 v207, 31, v206
	v_lshl_add_u64 v[196:197], s[44:45], 0, v[196:197]
	v_lshlrev_b64 v[208:209], 11, v[206:207]
	v_lshl_add_u64 v[208:209], v[196:197], 0, v[208:209]
	global_store_dwordx4 v[208:209], v[202:205], off nt
	v_mul_f32_e32 v132, 0x42000000, v137
	v_mul_f32_e32 v136, 0x42000000, v145
	v_mul_f32_e32 v202, 0x42000000, v133
	v_cvt_pk_fp8_f32 v202, v202, v132
	v_mul_f32_e32 v203, 0x42000000, v141
	v_cvt_pk_fp8_f32 v203, v203, v136
	v_mul_f32_e32 v132, 0x42000000, v193
	v_mul_f32_e32 v133, 0x42000000, v153
	v_cvt_pk_fp8_f32 v202, v132, v133 op_sel:[0,0,1]
	v_mul_f32_e32 v132, 0x42000000, v149
	v_mul_f32_e32 v133, 0x42000000, v157
	v_cvt_pk_fp8_f32 v203, v132, v133 op_sel:[0,0,1]
	v_mul_f32_e32 v204, 0x42000000, v161
	v_mul_f32_e32 v132, 0x42000000, v165
	v_cvt_pk_fp8_f32 v204, v204, v132
	v_mul_f32_e32 v205, 0x42000000, v177
	v_mul_f32_e32 v136, 0x42000000, v185
	v_cvt_pk_fp8_f32 v205, v205, v136
	v_mul_f32_e32 v132, 0x42000000, v169
	v_mul_f32_e32 v133, 0x42000000, v173
	v_cvt_pk_fp8_f32 v204, v132, v133 op_sel:[0,0,1]
	v_mul_f32_e32 v132, 0x42000000, v181
	v_mul_f32_e32 v133, 0x42000000, v189
	v_cvt_pk_fp8_f32 v205, v132, v133 op_sel:[0,0,1]
	v_or_b32_e32 v132, 1, v206
	v_ashrrev_i32_e32 v133, 31, v132
	v_lshlrev_b64 v[132:133], 11, v[132:133]
	v_lshl_add_u64 v[132:133], v[196:197], 0, v[132:133]
	global_store_dwordx4 v[132:133], v[202:205], off nt
	v_mul_f32_e32 v132, 0x42000000, v138
	v_mul_f32_e32 v133, 0x42000000, v154
	v_mul_f32_e32 v202, 0x42000000, v134
	v_cvt_pk_fp8_f32 v202, v202, v132
	v_mul_f32_e32 v203, 0x42000000, v142
	v_mul_f32_e32 v134, 0x42000000, v146
	v_cvt_pk_fp8_f32 v203, v203, v134
	v_mul_f32_e32 v132, 0x42000000, v194
	v_cvt_pk_fp8_f32 v202, v132, v133 op_sel:[0,0,1]
	v_mul_f32_e32 v132, 0x42000000, v150
	v_mul_f32_e32 v133, 0x42000000, v158
	v_cvt_pk_fp8_f32 v203, v132, v133 op_sel:[0,0,1]
	v_mul_f32_e32 v204, 0x42000000, v162
	v_mul_f32_e32 v132, 0x42000000, v166
	v_cvt_pk_fp8_f32 v204, v204, v132
	v_mul_f32_e32 v205, 0x42000000, v178
	v_mul_f32_e32 v134, 0x42000000, v186
	v_cvt_pk_fp8_f32 v205, v205, v134
	v_mul_f32_e32 v132, 0x42000000, v170
	v_mul_f32_e32 v133, 0x42000000, v174
	v_cvt_pk_fp8_f32 v204, v132, v133 op_sel:[0,0,1]
	v_mul_f32_e32 v132, 0x42000000, v182
	v_mul_f32_e32 v133, 0x42000000, v190
	v_cvt_pk_fp8_f32 v205, v132, v133 op_sel:[0,0,1]
	v_or_b32_e32 v132, 2, v206
	v_ashrrev_i32_e32 v133, 31, v132
	v_lshlrev_b64 v[132:133], 11, v[132:133]
	v_lshl_add_u64 v[132:133], v[196:197], 0, v[132:133]
	global_store_dwordx4 v[132:133], v[202:205], off nt
	v_mul_f32_e32 v132, 0x42000000, v135
	v_mul_f32_e32 v133, 0x42000000, v139
	v_cvt_pk_fp8_f32 v132, v132, v133
	v_mul_f32_e32 v133, 0x42000000, v143
	v_mul_f32_e32 v136, 0x42000000, v147
	v_cvt_pk_fp8_f32 v133, v133, v136
	v_mul_f32_e32 v134, 0x42000000, v195
	v_mul_f32_e32 v135, 0x42000000, v155
	v_cvt_pk_fp8_f32 v132, v134, v135 op_sel:[0,0,1]
	v_mul_f32_e32 v134, 0x42000000, v151
	v_mul_f32_e32 v135, 0x42000000, v159
	v_cvt_pk_fp8_f32 v133, v134, v135 op_sel:[0,0,1]
	v_mul_f32_e32 v134, 0x42000000, v163
	v_mul_f32_e32 v135, 0x42000000, v167
	v_cvt_pk_fp8_f32 v134, v134, v135
	v_mul_f32_e32 v135, 0x42000000, v179
	v_mul_f32_e32 v138, 0x42000000, v187
	v_cvt_pk_fp8_f32 v135, v135, v138
	v_mul_f32_e32 v136, 0x42000000, v171
	v_mul_f32_e32 v137, 0x42000000, v175
	v_cvt_pk_fp8_f32 v134, v136, v137 op_sel:[0,0,1]
	v_mul_f32_e32 v136, 0x42000000, v183
	v_mul_f32_e32 v137, 0x42000000, v191
	v_cvt_pk_fp8_f32 v135, v136, v137 op_sel:[0,0,1]
	v_or_b32_e32 v136, 3, v206
	v_ashrrev_i32_e32 v137, 31, v136
	v_lshlrev_b64 v[136:137], 11, v[136:137]
	v_lshl_add_u64 v[136:137], v[196:197], 0, v[136:137]
	s_andn2_b64 vcc, exec, s[10:11]
	global_store_dwordx4 v[136:137], v[132:135], off nt
	s_cbranch_vccz .LBB0_497
	s_andn2_b64 vcc, exec, s[88:89]
	s_cbranch_vccnz .LBB0_490
	s_branch .LBB0_498

	.amdhsa_kernel _ZN12_GLOBAL__N_16k_megaENS_6ParamsE
		.amdhsa_group_segment_fixed_size 0
		.amdhsa_private_segment_fixed_size 0
		.amdhsa_kernarg_size 720
		.amdhsa_user_sgpr_count 2
		.amdhsa_user_sgpr_dispatch_ptr 0
		.amdhsa_user_sgpr_queue_ptr 0
		.amdhsa_user_sgpr_kernarg_segment_ptr 1
		.amdhsa_user_sgpr_dispatch_id 0
		.amdhsa_user_sgpr_kernarg_preload_length 0
		.amdhsa_user_sgpr_kernarg_preload_offset 0
		.amdhsa_user_sgpr_private_segment_size 0
		.amdhsa_uses_dynamic_stack 0
		.amdhsa_enable_private_segment 0
		.amdhsa_system_sgpr_workgroup_id_x 1
		.amdhsa_system_sgpr_workgroup_id_y 0
		.amdhsa_system_sgpr_workgroup_id_z 0
		.amdhsa_system_sgpr_workgroup_info 0
		.amdhsa_system_vgpr_workitem_id 0
		.amdhsa_next_free_vgpr 256
		.amdhsa_next_free_sgpr 102
		.amdhsa_accum_offset 256
		.amdhsa_reserve_vcc 1
		.amdhsa_float_round_mode_32 0
		.amdhsa_float_round_mode_16_64 0
		.amdhsa_float_denorm_mode_32 3
		.amdhsa_float_denorm_mode_16_64 3
		.amdhsa_dx10_clamp 1
		.amdhsa_ieee_mode 1
		.amdhsa_fp16_overflow 0
		.amdhsa_tg_split 0
		.amdhsa_exception_fp_ieee_invalid_op 0
		.amdhsa_exception_fp_denorm_src 0
		.amdhsa_exception_fp_ieee_div_zero 0
		.amdhsa_exception_fp_ieee_overflow 0
		.amdhsa_exception_fp_ieee_underflow 0
		.amdhsa_exception_fp_ieee_inexact 0
		.amdhsa_exception_int_div_zero 0
	.end_amdhsa_kernel

amdhsa.kernels:
  - .agpr_count:     0
    .args:
      - .offset:         0
        .size:           464
        .value_kind:     by_value
      - .offset:         464
        .size:           4
        .value_kind:     hidden_block_count_x
      - .offset:         468
        .size:           4
        .value_kind:     hidden_block_count_y
      - .offset:         472
        .size:           4
        .value_kind:     hidden_block_count_z
      - .offset:         476
        .size:           2
        .value_kind:     hidden_group_size_x
      - .offset:         478
        .size:           2
        .value_kind:     hidden_group_size_y
      - .offset:         480
        .size:           2
        .value_kind:     hidden_group_size_z
      - .offset:         482
        .size:           2
        .value_kind:     hidden_remainder_x
      - .offset:         484
        .size:           2
        .value_kind:     hidden_remainder_y
      - .offset:         486
        .size:           2
        .value_kind:     hidden_remainder_z
      - .offset:         504
        .size:           8
        .value_kind:     hidden_global_offset_x
      - .offset:         512
        .size:           8
        .value_kind:     hidden_global_offset_y
      - .offset:         520
        .size:           8
        .value_kind:     hidden_global_offset_z
      - .offset:         528
        .size:           2
        .value_kind:     hidden_grid_dims
      - .offset:         584
        .size:           4
        .value_kind:     hidden_dynamic_lds_size
    .group_segment_fixed_size: 0
    .kernarg_segment_align: 8
    .kernarg_segment_size: 720
    .language:       OpenCL C
    .language_version:
      - 2
      - 0
    .max_flat_workgroup_size: 512
    .name:           _ZN12_GLOBAL__N_16k_megaENS_6ParamsE
    .private_segment_fixed_size: 0
    .sgpr_count:     108
    .sgpr_spill_count: 20
    .symbol:         _ZN12_GLOBAL__N_16k_megaENS_6ParamsE.kd
    .uniform_work_group_size: 1
    .uses_dynamic_stack: false
    .vgpr_count:     256
    .vgpr_spill_count: 0
    .wavefront_size: 64
